# P0 S5 unit: B-bar and C operand loads of both loop iterations issued up front with the first loads (12 loads in flight, 6 dependent round trips removed)
# speedup vs baseline: 1.0073x; 1.0073x over previous
; DI const float* inp(kptr_t k, int i) { return (const float*)k[i]; }
; DI double exp_d(double x) {
;     const double kf = __builtin_rint(x * 1.4426950408889634); const double r = x - kf * 0.6931471805599453094;
;     double t = 1.0, s = 1.0;
; #pragma unroll
;     for (int i = 1; i <= 16; ++i) { t *= r * (1.0 / (double)i); s += t; }
;     const int k = (int)kf;
;     return __builtin_ldexp(s, k);
; }
; DI void p_ssm_unit(Frame& F, int unit) {
;     ...
;     const double dt = exp_d((double)inp(KA, I_LOGDT)[lg]);
;     for (int i = F.tid; i < 33 * 64; i += 512) { const int tau = i >> 6, p = i & 63;
;         const double lre = fmin((double)inp(KA, I_ARE)[lg * SP + p], -1e-4), lim = (double)inp(KA, I_AIM)[lg * SP + p];
;         const double mag = exp_d(lre * dt * (double)tau); double sn, cs; sincos_d(lim * dt * (double)tau, sn, cs);
;         Lp[i * 2] = mag * cs; Lp[i * 2 + 1] = mag * sn; }
;     __syncthreads();
;     for (int i = F.tid; i < SP * SG; i += 512) { const int p = i >> 4, cc = i & 15;
;         const double lre = fmin((double)inp(KA, I_ARE)[lg * SP + p], -1e-4), lim = (double)inp(KA, I_AIM)[lg * SP + p];
;         const double nre = Lp[(64 + p) * 2] - 1.0, nim = Lp[(64 + p) * 2 + 1], den = lre * lre + lim * lim;
;         const double zre = (nre * lre + nim * lim) / den, zim = (nim * lre - nre * lim) / den;
;         const double br = (double)inp(KA, I_BRE)[((size_t)lg * SP + p) * SG + cc], bi = (double)inp(KA, I_BIM)[((size_t)lg * SP + p) * SG + cc];
;         Bb[i * 2] = (float)(zre * br - zim * bi); Bb[i * 2 + 1] = (float)(zre * bi + zim * br); }
;     for (int i = F.tid; i < SG * SP; i += 512) { Cc[i * 2] = inp(KA, I_CRE)[(size_t)lg * SG * SP + i]; Cc[i * 2 + 1] = inp(KA, I_CIM)[(size_t)lg * SG * SP + i]; }
.LBB0_17:
	s_and_b64 vcc, exec, s[4:5]
	s_cbranch_vccz .LBB0_76
	s_mov_b32 s97, s12
	s_mov_b32 s4, -1
	s_lshl_b32 s44, s97, 6
	v_mbcnt_lo_u32_b32 v0, s4, 0
	v_mbcnt_hi_u32_b32 v20, s4, v0
	v_readlane_b32 s4, v253, 29
	v_readlane_b32 s5, v253, 30
	v_add_u32_e32 v10, s44, v20
	s_mov_b32 s14, 0x6dc9c883
	v_readlane_b32 s90, v253, 6
	s_movk_i32 s4, 0x840
	s_mov_b32 s15, 0x3fc45f30
	v_readlane_b32 s91, v253, 7
	s_ashr_i32 s89, s88, 31
	v_cmp_gt_i32_e64 s[4:5], s4, v10
	s_and_saveexec_b64 s[6:7], s[4:5]
	s_cbranch_execz .LBB0_21
	s_load_dwordx2 s[8:9], s[90:91], 0x60
	s_lshl_b64 s[10:11], s[88:89], 2
	s_mov_b32 s70, s18
	s_mov_b32 s72, s16
	s_mov_b32 s74, s20
	s_waitcnt lgkmcnt(0)
	s_add_u32 s8, s8, s10
	s_addc_u32 s9, s9, s11
	global_load_dword v4, v9, s[8:9]
	s_load_dwordx4 s[8:11], s[90:91], 0x50
	s_lshl_b32 s12, s88, 6
	v_and_or_b32 v0, v20, 63, s12
	v_ashrrev_i32_e32 v1, 31, v0
	v_lshlrev_b64 v[0:1], 2, v[0:1]
	s_waitcnt lgkmcnt(0)
	v_lshl_add_u64 v[2:3], s[8:9], 0, v[0:1]
	v_lshl_add_u64 v[0:1], s[10:11], 0, v[0:1]
	global_load_dword v11, v[2:3], off
	global_load_dword v21, v[0:1], off
	v_lshrrev_b32_e32 v252, 4, v10
	v_lshlrev_b32_e32 v252, 2, v252
	s_lshl_b32 s98, s88, 8
	s_add_u32 s8, s8, s98
	s_addc_u32 s9, s9, 0
	s_add_u32 s10, s10, s98
	s_addc_u32 s11, s11, 0
	global_load_dword v240, v252, s[8:9]
	global_load_dword v241, v252, s[10:11]
	global_load_dword v242, v252, s[8:9] offset:128
	global_load_dword v243, v252, s[10:11] offset:128
	s_load_dwordx4 s[8:11], s[90:91], 0x68
	v_lshlrev_b32_e32 v252, 2, v10
	s_lshl_b32 s98, s88, 12
	s_waitcnt lgkmcnt(0)
	s_add_u32 s8, s8, s98
	s_addc_u32 s9, s9, 0
	s_add_u32 s10, s10, s98
	s_addc_u32 s11, s11, 0
	global_load_dword v244, v252, s[10:11]
	global_load_dword v245, v252, s[8:9]
	global_load_dword v246, v252, s[10:11] offset:2048
	global_load_dword v247, v252, s[8:9] offset:2048
	s_load_dwordx4 s[8:11], s[90:91], 0x78
	s_waitcnt lgkmcnt(0)
	s_add_u32 s8, s8, s98
	s_addc_u32 s9, s9, 0
	s_add_u32 s10, s10, s98
	s_addc_u32 s11, s11, 0
	global_load_dword v248, v252, s[8:9]
	global_load_dword v249, v252, s[10:11]
	global_load_dword v250, v252, s[8:9] offset:2048
	global_load_dword v251, v252, s[10:11] offset:2048
	s_mov_b32 s76, s22
	s_mov_b32 s78, s18
	s_mov_b32 s80, s16
	s_mov_b32 s82, s20
	s_mov_b32 s84, s28
	s_lshl_b32 s10, s97, 10
	s_add_i32 s10, s10, 0
	s_mov_b64 s[8:9], 0
	v_lshl_add_u32 v8, v20, 4, s10
	s_waitcnt vmcnt(14)
	v_cvt_f64_f32_e32 v[0:1], v4
	v_mul_f64 v[2:3], v[0:1], s[0:1]
	v_rndne_f64_e32 v[2:3], v[2:3]
	v_fmac_f64_e32 v[0:1], s[2:3], v[2:3]
	v_cvt_i32_f64_e32 v24, v[2:3]
	v_add_f64 v[2:3], v[0:1], 1.0
	v_mul_f64 v[4:5], v[0:1], 0.5
	v_mul_f64 v[6:7], v[0:1], s[16:17]
	v_mul_f64 v[46:47], v[0:1], v[4:5]
	v_fmac_f64_e32 v[2:3], v[0:1], v[4:5]
	v_ldexp_f64 v[12:13], v[0:1], -2
	v_mul_f64 v[4:5], v[6:7], v[46:47]
	v_fmac_f64_e32 v[2:3], v[6:7], v[46:47]
	v_mul_f64 v[14:15], v[0:1], s[70:71]
	v_mul_f64 v[6:7], v[12:13], v[4:5]
	v_fmac_f64_e32 v[2:3], v[12:13], v[4:5]
	v_mul_f64 v[16:17], v[0:1], s[72:73]
	v_mul_f64 v[4:5], v[14:15], v[6:7]
	v_fmac_f64_e32 v[2:3], v[14:15], v[6:7]
	v_mul_f64 v[18:19], v[0:1], s[74:75]
	v_mul_f64 v[6:7], v[16:17], v[4:5]
	v_fmac_f64_e32 v[2:3], v[16:17], v[4:5]
	v_ldexp_f64 v[22:23], v[0:1], -3
	v_mul_f64 v[4:5], v[18:19], v[6:7]
	v_fmac_f64_e32 v[2:3], v[18:19], v[6:7]
	v_mul_f64 v[26:27], v[0:1], s[76:77]
	v_mul_f64 v[6:7], v[22:23], v[4:5]
	v_fmac_f64_e32 v[2:3], v[22:23], v[4:5]
	v_mul_f64 v[28:29], v[0:1], s[78:79]
	v_mul_f64 v[4:5], v[26:27], v[6:7]
	v_fmac_f64_e32 v[2:3], v[26:27], v[6:7]
	v_mul_f64 v[30:31], v[0:1], s[24:25]
	v_mul_f64 v[6:7], v[28:29], v[4:5]
	v_fmac_f64_e32 v[2:3], v[28:29], v[4:5]
	v_mul_f64 v[32:33], v[0:1], s[80:81]
	v_mul_f64 v[4:5], v[30:31], v[6:7]
	v_fmac_f64_e32 v[2:3], v[30:31], v[6:7]
	v_mul_f64 v[34:35], v[0:1], s[26:27]
	v_mul_f64 v[6:7], v[32:33], v[4:5]
	v_fmac_f64_e32 v[2:3], v[32:33], v[4:5]
	v_mul_f64 v[36:37], v[0:1], s[82:83]
	v_mul_f64 v[4:5], v[34:35], v[6:7]
	v_fmac_f64_e32 v[2:3], v[34:35], v[6:7]
	v_mul_f64 v[38:39], v[0:1], s[84:85]
	v_mul_f64 v[6:7], v[36:37], v[4:5]
	v_fmac_f64_e32 v[2:3], v[36:37], v[4:5]
	v_ldexp_f64 v[40:41], v[0:1], -4
	v_mul_f64 v[4:5], v[38:39], v[6:7]
	v_fmac_f64_e32 v[2:3], v[38:39], v[6:7]
	s_waitcnt vmcnt(13)
	v_cvt_f64_f32_e32 v[42:43], v11
	v_fmac_f64_e32 v[2:3], v[40:41], v[4:5]
	s_waitcnt vmcnt(12)
	v_cvt_f64_f32_e32 v[44:45], v21
	v_min_f64 v[0:1], v[42:43], s[30:31]
	v_ldexp_f64 v[2:3], v[2:3], v24
	v_mul_f64 v[0:1], v[0:1], v[2:3]
	v_mul_f64 v[2:3], v[2:3], v[44:45]
	v_mov_b32_e32 v11, v10

; DI const float* inp(kptr_t k, int i) { return (const float*)k[i]; }
; DI void p_ssm_unit(Frame& F, int unit) {
;     ...
;     for (int i = F.tid; i < SP * SG; i += 512) { const int p = i >> 4, cc = i & 15;
;         const double lre = fmin((double)inp(KA, I_ARE)[lg * SP + p], -1e-4), lim = (double)inp(KA, I_AIM)[lg * SP + p];
;         const double nre = Lp[(64 + p) * 2] - 1.0, nim = Lp[(64 + p) * 2 + 1], den = lre * lre + lim * lim;
;         const double zre = (nre * lre + nim * lim) / den, zim = (nim * lre - nre * lim) / den;
;         const double br = (double)inp(KA, I_BRE)[((size_t)lg * SP + p) * SG + cc], bi = (double)inp(KA, I_BIM)[((size_t)lg * SP + p) * SG + cc];
;         Bb[i * 2] = (float)(zre * br - zim * bi); Bb[i * 2 + 1] = (float)(zre * bi + zim * br); }
;     for (int i = F.tid; i < SG * SP; i += 512) { Cc[i * 2] = inp(KA, I_CRE)[(size_t)lg * SG * SP + i]; Cc[i * 2 + 1] = inp(KA, I_CIM)[(size_t)lg * SG * SP + i]; }
.LBB0_23:
	v_ashrrev_i32_e32 v12, 4, v3
	v_add_u32_e32 v4, s66, v12
	v_ashrrev_i32_e32 v5, 31, v4
	v_lshlrev_b64 v[4:5], 2, v[4:5]
	s_waitcnt lgkmcnt(0)
	v_lshl_add_u64 v[6:7], s[8:9], 0, v[4:5]
	v_lshl_add_u64 v[4:5], s[10:11], 0, v[4:5]
	v_mov_b32_e32 v4, v241
	v_ashrrev_i32_e32 v13, 31, v12
	v_mov_b32_e32 v6, v240
	s_waitcnt vmcnt(0)
	v_cvt_f64_f32_e32 v[16:17], v4
	v_and_b32_e32 v4, -16, v3
	s_waitcnt vmcnt(0)
	v_cvt_f64_f32_e32 v[6:7], v6
	v_add_u32_e32 v4, 0, v4
	v_min_f64 v[14:15], v[6:7], s[30:31]
	ds_read_b128 v[4:7], v4 offset:1024
	v_mul_f64 v[18:19], v[16:17], v[16:17]
	v_fmac_f64_e32 v[18:19], v[14:15], v[14:15]
	s_waitcnt lgkmcnt(0)
	v_add_f64 v[4:5], v[4:5], -1.0
	v_mul_f64 v[22:23], v[6:7], v[16:17]
	v_fmac_f64_e32 v[22:23], v[14:15], v[4:5]
	v_div_scale_f64 v[26:27], s[96:97], v[18:19], v[18:19], v[22:23]
	v_rcp_f64_e32 v[28:29], v[26:27]
	v_mul_f64 v[4:5], v[4:5], v[16:17]
	v_fma_f64 v[4:5], v[14:15], v[6:7], -v[4:5]
	v_div_scale_f64 v[6:7], s[96:97], v[18:19], v[18:19], v[4:5]
	v_rcp_f64_e32 v[14:15], v[6:7]
	v_fma_f64 v[30:31], -v[26:27], v[28:29], 1.0
	v_fmac_f64_e32 v[28:29], v[28:29], v[30:31]
	v_fma_f64 v[30:31], -v[26:27], v[28:29], 1.0
	v_fmac_f64_e32 v[28:29], v[28:29], v[30:31]
	v_div_scale_f64 v[30:31], vcc, v[22:23], v[18:19], v[22:23]
	v_fma_f64 v[16:17], -v[6:7], v[14:15], 1.0
	v_mul_f64 v[32:33], v[30:31], v[28:29]
	v_fmac_f64_e32 v[14:15], v[14:15], v[16:17]
	v_fma_f64 v[26:27], -v[26:27], v[32:33], v[30:31]
	v_fma_f64 v[16:17], -v[6:7], v[14:15], 1.0
	v_div_fmas_f64 v[26:27], v[26:27], v[28:29], v[32:33]
	v_fmac_f64_e32 v[14:15], v[14:15], v[16:17]
	v_div_scale_f64 v[16:17], vcc, v[4:5], v[18:19], v[4:5]
	v_div_fixup_f64 v[22:23], v[26:27], v[18:19], v[22:23]
	v_mul_f64 v[26:27], v[16:17], v[14:15]
	v_fma_f64 v[6:7], -v[6:7], v[26:27], v[16:17]
	s_nop 0
	v_div_fmas_f64 v[6:7], v[6:7], v[14:15], v[26:27]
	v_div_fixup_f64 v[4:5], v[6:7], v[18:19], v[4:5]
	v_lshl_add_u64 v[6:7], v[12:13], 4, v[0:1]
	v_lshlrev_b64 v[6:7], 2, v[6:7]
	v_lshl_add_u64 v[12:13], s[12:13], 0, v[6:7]
	v_lshl_add_u64 v[6:7], s[14:15], 0, v[6:7]
	v_mov_b32_e32 v6, v244
	v_cmp_lt_i32_e32 vcc, s64, v3
	v_mov_b32_e32 v8, v245
	s_or_b64 s[6:7], vcc, s[6:7]
	s_waitcnt vmcnt(1)
	v_cvt_f64_f32_e32 v[6:7], v6
	v_mul_f64 v[14:15], v[4:5], v[6:7]
	s_waitcnt vmcnt(0)
	v_cvt_f64_f32_e32 v[12:13], v8
	v_mul_f64 v[6:7], v[22:23], v[6:7]
	v_fma_f64 v[14:15], v[22:23], v[12:13], -v[14:15]
	v_fmac_f64_e32 v[6:7], v[4:5], v[12:13]
	v_cvt_f32_f64_e32 v14, v[14:15]
	v_cvt_f32_f64_e32 v15, v[6:7]
	v_add_u32_e32 v4, 0x200, v3
	ds_write_b64 v2, v[14:15]
	v_add_u32_e32 v2, 0x1000, v2
	v_mov_b32_e32 v3, v4
	v_mov_b32_e32 v240, v242
	v_mov_b32_e32 v241, v243
	v_mov_b32_e32 v244, v246
	v_mov_b32_e32 v245, v247
	s_andn2_b64 exec, exec, s[6:7]
	s_cbranch_execnz .LBB0_23
	s_or_b64 exec, exec, s[6:7]
	s_load_dwordx4 s[8:11], s[90:91], 0x78
	v_max_i32_e32 v0, 0x200, v10
	v_sub_u32_e32 v0, v0, v10
	v_add_u32_e32 v1, 0x1ff, v0
	s_movk_i32 s6, 0x2200
	v_cmp_gt_u32_e64 s[12:13], s6, v1
	s_movk_i32 s6, 0x21ff
	v_cmp_lt_u32_e32 vcc, s6, v1
	v_mov_b32_e32 v0, v10
	s_and_saveexec_b64 s[14:15], vcc
	s_cbranch_execz .LBB0_35
	v_add_u32_e32 v0, s45, v21
	v_lshlrev_b32_e32 v2, 3, v1
	v_add_u32_e32 v0, 0xc404, v0
	v_and_b32_e32 v2, 0xfffff000, v2
	s_brev_b32 s6, 4
	v_add_u32_e32 v2, v0, v2
	v_cmp_gt_u32_e32 vcc, s6, v1
	v_cmp_ge_u32_e64 s[6:7], v2, v0
	s_and_b64 s[96:97], s[6:7], vcc
	s_mov_b64 s[66:67], -1
	v_mov_b32_e32 v0, v10
	s_and_saveexec_b64 s[6:7], s[96:97]
	s_cbranch_execz .LBB0_34
	v_lshrrev_b32_e32 v2, 9, v1
	v_add_u32_e32 v0, -1, v2
	v_add_u32_e32 v11, 0x200, v10
	v_lshrrev_b32_e32 v1, 1, v0
	v_add_u32_e32 v3, 1, v1
	v_cmp_lt_u32_e32 vcc, 5, v0
	v_mov_b64_e32 v[0:1], v[10:11]
	s_and_saveexec_b64 s[96:97], vcc
	s_cbranch_execz .LBB0_30
	v_and_b32_e32 v4, -4, v3
	s_mov_b64 s[66:67], 0
	v_mov_b64_e32 v[0:1], v[10:11]

; DI const float* inp(kptr_t k, int i) { return (const float*)k[i]; }
; DI void p_ssm_unit(Frame& F, int unit) {
;     ...
;     for (int i = F.tid; i < SG * SP; i += 512) { Cc[i * 2] = inp(KA, I_CRE)[(size_t)lg * SG * SP + i]; Cc[i * 2 + 1] = inp(KA, I_CIM)[(size_t)lg * SG * SP + i]; }
.LBB0_37:
	v_mov_b32_e32 v6, v248
	v_mov_b32_e32 v7, v249
	v_add_u32_e32 v4, 0x200, v4
	v_cmp_lt_i32_e32 vcc, s64, v4
	v_lshl_add_u64 v[0:1], v[0:1], 0, s[68:69]
	v_lshl_add_u64 v[2:3], v[2:3], 0, s[68:69]
	s_or_b64 s[6:7], vcc, s[6:7]
	s_waitcnt vmcnt(0)
	ds_write_b64 v5, v[6:7]
	v_add_u32_e32 v5, 0x1000, v5
	v_mov_b32_e32 v248, v250
	v_mov_b32_e32 v249, v251
	s_andn2_b64 exec, exec, s[6:7]
	s_cbranch_execnz .LBB0_37
